# barrier: leaders poll TOP counter directly (one fewer dependent round trip); pro_c barrier dropped; wbl2 skipped after write-through-only phases
# speedup vs baseline: 1.0247x; 1.0054x over previous
.LBB0_118:
	s_or_b64 exec, exec, s[6:7]
	v_cvt_f32_u32_e32 v3, v0
	s_waitcnt vmcnt(0)
	v_readfirstlane_b32 s4, v2
	s_add_u32 s6, s60, 0x3500
	s_addc_u32 s7, s61, 0
	v_rcp_iflag_f32_e32 v3, v3
	v_add_u32_e32 v1, s4, v1
	v_add_u32_e32 v4, 1, v1
	s_mov_b64 s[8:9], -1
	v_mul_f32_e32 v2, 0x4f7ffffe, v3
	v_cvt_u32_f32_e32 v2, v2
	v_sub_u32_e32 v3, 0, v0
	v_mul_lo_u32 v3, v3, v2
	v_mul_hi_u32 v3, v2, v3
	v_add_u32_e32 v2, v2, v3
	v_mul_hi_u32 v2, v1, v2
	v_mul_lo_u32 v3, v2, v0
	v_sub_u32_e32 v1, v1, v3
	v_add_u32_e32 v5, 1, v2
	v_cmp_ge_u32_e32 vcc, v1, v0
	v_sub_u32_e32 v3, v1, v0
	s_nop 0
	v_cndmask_b32_e32 v2, v2, v5, vcc
	v_cndmask_b32_e32 v1, v1, v3, vcc
	v_add_u32_e32 v3, 1, v2
	v_cmp_ge_u32_e32 vcc, v1, v0
	s_nop 1
	v_cndmask_b32_e32 v2, v2, v3, vcc
	v_mad_u64_u32 v[0:1], s[4:5], v0, v2, v[0:1]
	v_mov_b32_e32 v20, v0
	v_cmp_ne_u32_e32 vcc, v4, v0
	v_mov_b64_e32 v[0:1], s[6:7]
	s_and_saveexec_b64 s[4:5], vcc
	s_cbranch_execz .LBB0_130
	v_mov_b32_e32 v0, 0
	global_load_dword v1, v0, s[6:7] offset:-256 sc1
	s_mov_b64 s[12:13], 0
	s_waitcnt vmcnt(0)
	v_cmp_gt_u32_e32 vcc, v20, v1
	s_and_saveexec_b64 s[10:11], vcc
	s_cbranch_execz .LBB0_129
	s_add_u32 s8, s60, 0x200
	s_addc_u32 s9, s61, 0
	s_mov_b32 s22, 1
	s_branch .LBB0_122

.LBB0_124:
	global_load_dword v1, v0, s[6:7] offset:-256 sc1
	s_add_i32 s22, s22, 1
	s_mov_b64 s[16:17], -1
	s_waitcnt vmcnt(0)
	v_cmp_le_u32_e32 vcc, v20, v1
	s_orn2_b64 s[20:21], vcc, exec
	s_branch .LBB0_121

.LBB0_282:
	s_cmp_lt_i32 s29, 4
	s_branch .LBB0_336
	s_getreg_b32 s2, hwreg(HW_REG_XCC_ID, 0, 4)
	v_readlane_b32 s0, v250, 4
	s_waitcnt vmcnt(0)
	v_mov_b32 v1, s0
	s_waitcnt vmcnt(0)
	s_barrier
	s_cmp_eq_u32 s43, 1
	s_cbranch_scc0 .Learlyinv_2
	buffer_inv sc1
	s_waitcnt vmcnt(0)

.LBB0_488:
	s_or_b64 exec, exec, s[8:9]
	s_waitcnt vmcnt(0)
	v_readfirstlane_b32 s1, v2
	v_cvt_f32_u32_e32 v2, v0
	v_sub_u32_e32 v3, 0, v0
	v_add_u32_e32 v1, s1, v1
	v_rcp_iflag_f32_e32 v2, v2
	s_nop 0
	v_mul_f32_e32 v2, 0x4f7ffffe, v2
	v_cvt_u32_f32_e32 v2, v2
	v_mul_lo_u32 v3, v3, v2
	v_mul_hi_u32 v3, v2, v3
	v_add_u32_e32 v2, v2, v3
	v_mul_hi_u32 v2, v1, v2
	v_mul_lo_u32 v3, v2, v0
	v_sub_u32_e32 v3, v1, v3
	v_cmp_ge_u32_e32 vcc, v3, v0
	v_add_u32_e32 v4, 1, v2
	s_nop 0
	v_cndmask_b32_e32 v2, v2, v4, vcc
	v_sub_u32_e32 v4, v3, v0
	v_cndmask_b32_e32 v3, v3, v4, vcc
	v_cmp_ge_u32_e32 vcc, v3, v0
	v_add_u32_e32 v3, 1, v2
	s_nop 0
	v_cndmask_b32_e32 v2, v2, v3, vcc
	v_add_u32_e32 v3, 1, v1
	v_readlane_b32 s0, v250, 35
	v_mad_u64_u32 v[0:1], s[2:3], v0, v2, v[0:1]
	v_mov_b32_e32 v20, v0
	v_readlane_b32 s1, v250, 36
	v_cmp_ne_u32_e32 vcc, v3, v0
	s_mov_b64 s[2:3], -1
	v_mov_b64_e32 v[0:1], s[0:1]
	s_and_saveexec_b64 s[8:9], vcc
	s_cbranch_execz .LBB0_500
	v_readlane_b32 s0, v250, 35
	v_readlane_b32 s1, v250, 36
	s_mov_b64 s[2:3], 0
	s_nop 3
	global_load_dword v0, v173, s[0:1] offset:-256 sc1
	s_waitcnt vmcnt(0)
	v_cmp_gt_u32_e32 vcc, v20, v0
	s_and_saveexec_b64 s[10:11], vcc
	s_cbranch_execz .LBB0_499
	s_mov_b32 s1, 1
	s_mov_b64 s[12:13], 0
	s_branch .LBB0_492

.LBB0_494:
	v_readlane_b32 s2, v250, 35
	v_readlane_b32 s3, v250, 36
	s_add_i32 s1, s1, 1
	s_mov_b64 s[18:19], -1
	s_nop 2
	global_load_dword v0, v173, s[2:3] offset:-256 sc1
	s_waitcnt vmcnt(0)
	v_cmp_le_u32_e32 vcc, v20, v0
	s_orn2_b64 s[16:17], vcc, exec
	s_branch .LBB0_491

.LBB0_617:
	s_andn2_saveexec_b64 s[2:3], s[8:9]
	s_cbranch_execz .LBB0_637
	s_mov_b64 s[2:3], exec
	s_waitcnt lgkmcnt(0)
	s_waitcnt vmcnt(0)
	v_mbcnt_lo_u32_b32 v1, s2, 0
	v_mbcnt_hi_u32_b32 v1, s3, v1
	v_cmp_eq_u32_e32 vcc, 0, v1
	s_and_saveexec_b64 s[8:9], vcc
	s_cbranch_execz .LBB0_620
	s_bcnt1_i32_b64 s2, s[2:3]
	v_mov_b32_e32 v2, s2
	v_readlane_b32 s2, v250, 33
	v_readlane_b32 s3, v250, 34
	s_nop 4
	global_atomic_add v2, v173, v2, s[2:3] sc0
.LBB0_620:
	s_or_b64 exec, exec, s[8:9]
	s_waitcnt vmcnt(0)
	v_readfirstlane_b32 s2, v2
	v_cvt_f32_u32_e32 v2, v0
	v_sub_u32_e32 v3, 0, v0
	v_add_u32_e32 v1, s2, v1
	v_readlane_b32 s8, v250, 35
	v_rcp_iflag_f32_e32 v2, v2
	v_readlane_b32 s9, v250, 36
	v_mul_f32_e32 v2, 0x4f7ffffe, v2
	v_cvt_u32_f32_e32 v2, v2
	v_mul_lo_u32 v3, v3, v2
	v_mul_hi_u32 v3, v2, v3
	v_add_u32_e32 v2, v2, v3
	v_mul_hi_u32 v2, v1, v2
	v_mul_lo_u32 v3, v2, v0
	v_sub_u32_e32 v3, v1, v3
	v_cmp_ge_u32_e32 vcc, v3, v0
	v_add_u32_e32 v4, 1, v2
	s_nop 0
	v_cndmask_b32_e32 v2, v2, v4, vcc
	v_sub_u32_e32 v4, v3, v0
	v_cndmask_b32_e32 v3, v3, v4, vcc
	v_cmp_ge_u32_e32 vcc, v3, v0
	v_add_u32_e32 v3, 1, v2
	s_nop 0
	v_cndmask_b32_e32 v2, v2, v3, vcc
	v_add_u32_e32 v3, 1, v1
	v_mad_u64_u32 v[0:1], s[2:3], v0, v2, v[0:1]
	v_mov_b32_e32 v20, v0
	v_cmp_ne_u32_e32 vcc, v3, v0
	s_mov_b64 s[2:3], -1
	v_mov_b64_e32 v[0:1], s[8:9]
	s_and_saveexec_b64 s[8:9], vcc
	s_cbranch_execz .LBB0_632
	v_readlane_b32 s2, v250, 35
	v_readlane_b32 s3, v250, 36
	s_nop 4
	global_load_dword v0, v173, s[2:3] offset:-256 sc1
	s_mov_b64 s[2:3], 0
	s_waitcnt vmcnt(0)
	v_cmp_gt_u32_e32 vcc, v20, v0
	s_and_saveexec_b64 s[10:11], vcc
	s_cbranch_execz .LBB0_631
	s_mov_b32 s20, 1
	s_mov_b64 s[12:13], 0
	s_branch .LBB0_624

.LBB0_626:
	v_readlane_b32 s2, v250, 35
	v_readlane_b32 s3, v250, 36
	s_add_i32 s20, s20, 1
	s_mov_b64 s[18:19], -1
	s_nop 2
	global_load_dword v0, v173, s[2:3] offset:-256 sc1
	s_waitcnt vmcnt(0)
	v_cmp_le_u32_e32 vcc, v20, v0
	s_orn2_b64 s[16:17], vcc, exec
	s_branch .LBB0_623

.LBB0_857:
	s_or_b64 exec, exec, s[4:5]
	s_waitcnt vmcnt(0)
	v_readfirstlane_b32 s2, v2
	v_cvt_f32_u32_e32 v2, v0
	v_sub_u32_e32 v3, 0, v0
	v_add_u32_e32 v1, s2, v1
	v_readlane_b32 s4, v250, 35
	v_rcp_iflag_f32_e32 v2, v2
	v_readlane_b32 s5, v250, 36
	v_mul_f32_e32 v2, 0x4f7ffffe, v2
	v_cvt_u32_f32_e32 v2, v2
	v_mul_lo_u32 v3, v3, v2
	v_mul_hi_u32 v3, v2, v3
	v_add_u32_e32 v2, v2, v3
	v_mul_hi_u32 v2, v1, v2
	v_mul_lo_u32 v3, v2, v0
	v_sub_u32_e32 v3, v1, v3
	v_cmp_ge_u32_e32 vcc, v3, v0
	v_add_u32_e32 v4, 1, v2
	s_nop 0
	v_cndmask_b32_e32 v2, v2, v4, vcc
	v_sub_u32_e32 v4, v3, v0
	v_cndmask_b32_e32 v3, v3, v4, vcc
	v_cmp_ge_u32_e32 vcc, v3, v0
	v_add_u32_e32 v3, 1, v2
	s_nop 0
	v_cndmask_b32_e32 v2, v2, v3, vcc
	v_add_u32_e32 v3, 1, v1
	v_mad_u64_u32 v[0:1], s[2:3], v0, v2, v[0:1]
	v_mov_b32_e32 v20, v0
	v_cmp_ne_u32_e32 vcc, v3, v0
	s_mov_b64 s[2:3], -1
	v_mov_b64_e32 v[0:1], s[4:5]
	s_and_saveexec_b64 s[4:5], vcc
	s_cbranch_execz .LBB0_869
	v_readlane_b32 s2, v250, 35
	v_readlane_b32 s3, v250, 36
	s_nop 4
	global_load_dword v0, v173, s[2:3] offset:-256 sc1
	s_mov_b64 s[2:3], 0
	s_waitcnt vmcnt(0)
	v_cmp_gt_u32_e32 vcc, v20, v0
	s_and_saveexec_b64 s[10:11], vcc
	s_cbranch_execz .LBB0_868
	s_mov_b32 s20, 1
	s_mov_b64 s[12:13], 0
	s_branch .LBB0_861
